# as v72 but the whole MoE-down e4m3 conversion stays in the attention trips (attention hosts 28 MoE-down + 56 fp6 items per wave, nothing hosted in the GEMM epilogues, no MoE conversion in P0)
# speedup vs baseline: 1.0189x; 1.0055x over previous
; #define RP(n) _Pragma("nounroll") for (int rep_ = 0; rep_ < (int)(((REPEAT) >> (n)) & 1u) + 1; ++rep_)
; __global__ void __launch_bounds__(NTHREADS, 2) fwd_kernel(Args args) {
;     ...
;     if (PH(15)) RP(15)
;     {
;         const int vcu = (G % 8 == 0) ? (bx % 8) * (G / 8) + bx / 8 : bx;
;         att::CvtState cs{args.in[I_MOED], ws + W_MOED, gw * att::CV_IPW, (gw + 1) * att::CV_IPW};
;         for (int L = vcu; L < NBATCH * NH * 8; L += G) {
.LBB0_1020:
	s_or_b64 exec, exec, s[4:5]
	s_lshr_b32 s0, s3, 29
	s_add_i32 s5, s2, s0
	s_and_b32 s0, s5, -8
	s_ashr_i32 s1, s76, 3
	s_sub_i32 s0, s2, s0
	s_mul_i32 s8, s1, s0
	s_ashr_i32 s1, s5, 3
	s_and_b32 s4, s76, 7
	s_add_i32 s5, s8, s1
	v_readlane_b32 s8, v251, 9
	s_add_u32 s30, s70, 0x24a00000
	s_mul_i32 s35, s8, 28
	s_addc_u32 s31, s71, 0
	s_add_i32 s50, s35, 28
	v_readlane_b32 s9, v251, 10
	s_add_u32 s8, s70, 0x4bc00000
	s_addc_u32 s9, s71, 0
	s_cmp_eq_u32 s4, 0
	s_cselect_b32 s51, s5, s2
	s_cmpk_gt_i32 s51, 0x1ff
	s_waitcnt lgkmcnt(0)
	s_barrier
	s_cbranch_scc1 .LBB0_1053
	s_add_u32 s4, s70, 0x3da00000
	s_addc_u32 s5, s71, 0
	s_add_u32 s10, s70, 0x3c200000
	s_addc_u32 s11, s71, 0
	s_movk_i32 s52, 0x2000
	s_mov_b32 s53, 0xc3e00000
	v_mov_b32_e32 v203, 0x43e00000
	v_mov_b32_e32 v191, 0
	s_movk_i32 s54, 0xd0
	s_movk_i32 s55, 0x3000
	s_mov_b32 s56, 0x5010400
	s_mov_b32 s57, 0x7030602
	s_mov_b32 s58, 0x5040100
	s_mov_b32 s59, 0x7060302
	s_add_i32 s60, 0, 0x6800
	s_movk_i32 s61, 0x1c00
	s_movk_i32 s62, 0x4000
	s_movk_i32 s63, 0x6000
	s_mov_b32 s64, 0x8000
	s_mov_b32 s65, 0xa000
	s_mov_b32 s66, 0xc000
	s_mov_b32 s67, 0xe000
	v_mov_b32_e32 v208, 0x1c00
	v_mov_b32_e32 v209, 0xff800000
	v_readlane_b32 s18, v251, 0
	v_readlane_b32 s19, v251, 1
	v_readlane_b32 s98, v251, 9
	s_nop 3
	s_sub_u32 s18, s18, 0x38
	s_subb_u32 s19, s19, 0
	s_load_dwordx4 s[44:47], s[18:19], 0x0
	s_mul_i32 s98, s98, 56
	s_add_i32 s99, s98, 56
	s_mov_b32 s100, 0
	s_waitcnt lgkmcnt(0)
	v_writelane_b32 v252, s44, 0
	v_writelane_b32 v252, s45, 1
	v_writelane_b32 v252, s46, 2
	v_writelane_b32 v252, s47, 3
	s_branch .LBB0_1023
